# quad-local chain from mixer final pass through router (5 grid barriers replaced by XCC-local 4-workgroup handoffs), attention LDS read pipelining, Q loads issued before the K wait
# speedup vs baseline: 1.0252x; 1.0113x over previous
.LBB0_790:
	s_add_u32 s0, s18, 0x4400
	s_addc_u32 s1, s19, 0
	v_mbcnt_hi_u32_b32 v0, -1, v217
	v_lshlrev_b32_e32 v1, 8, v0
	v_and_b32_e32 v1, 0x700, v1
	global_load_dword v2, v1, s[0:1] sc1
	v_mov_b32_e32 v3, 0x24a70
	ds_read_b32 v3, v3
	s_waitcnt vmcnt(0) lgkmcnt(0)
	s_getreg_b32 s0, hwreg(HW_REG_XCC_ID, 0, 4)
	v_cmp_eq_u32_e32 vcc, 32, v2
	s_nop 1
	s_cmp_eq_u64 vcc, exec
	s_cselect_b32 s100, 1, 0
	s_cmp_eq_u32 s38, 0x100
	s_cselect_b32 s100, s100, 0
	v_readfirstlane_b32 s1, v3
	s_nop 3
	s_lshl_b32 s98, s0, 3
	s_lshr_b32 s0, s1, 2
	s_add_i32 s98, s98, s0
	s_and_b32 s99, s1, 3
	s_cmp_eq_u32 s100, 1
	s_cbranch_scc0 .Lqo_p2c
	s_lshl_b32 s6, s98, 2
	s_add_i32 s6, s6, s99
	s_lshr_b32 s0, s98, 4
	s_lshl_b32 s0, s0, 9
	s_lshl_b32 s1, s99, 3
	s_add_i32 s1, s1, s88
	s_lshl_b32 s1, s1, 4
	s_add_i32 s36, s0, s1
	s_and_b32 s0, s98, 15
	s_add_i32 s36, s36, s0

.LBB0_827:
	s_cmp_eq_u32 s100, 1
	s_cbranch_scc1 .Lqs4
	s_cmp_gt_i32 s91, 5
	s_cselect_b64 s[2:3], -1, 0
	s_and_b64 s[0:1], s[4:5], s[2:3]
	s_andn2_b64 vcc, exec, s[0:1]
	s_cbranch_vccnz .LBB0_883
	s_cmp_gt_u32 s80, 63
	s_waitcnt lgkmcnt(0)
	s_mov_b64 s[8:9], 0
	s_cbranch_scc1 .LBB0_830
	v_mbcnt_hi_u32_b32 v0, -1, v217
	v_cmp_eq_u32_e32 vcc, 0, v0
	s_and_b64 s[8:9], vcc, exec

.Lqo_p4b2:
	s_bfe_i32 s1, s0, 0x80000
	s_bfe_u32 s1, s1, 0x5000a
	s_add_i32 s1, s0, s1
	s_bfe_i32 s1, s1, 0x80000
	s_sext_i32_i16 s1, s1
	s_ashr_i32 s13, s1, 5
	s_lshl_b32 s1, s13, 2
	s_add_i32 s2, s1, s12
	s_ashr_i32 s3, s2, 31
	s_lshl_b64 s[2:3], s[2:3], 17
	s_add_u32 s8, s58, s2
	s_addc_u32 s1, s59, s3
	s_and_b32 s9, s1, 0xffff
	s_ashr_i32 s1, s0, 31
	s_lshl_b64 s[0:1], s[0:1], 8
	v_lshl_add_u64 v[96:97], s[0:1], 0, v[128:129]
	s_lshl_b32 s0, s12, 8
	s_ashr_i32 s1, s0, 31
	s_lshl_b64 s[2:3], s[0:1], 1
	v_lshl_add_u64 v[98:99], v[132:133], 0, s[2:3]
	v_lshlrev_b64 v[138:139], 11, v[96:97]
	v_lshl_add_u64 v[4:5], v[98:99], 0, v[138:139]
	global_load_dwordx4 v[64:67], v[4:5], off
	global_load_dwordx4 v[68:71], v[4:5], off offset:64
	global_load_dwordx4 v[72:75], v[4:5], off offset:128
	global_load_dwordx4 v[76:79], v[4:5], off offset:192
	global_load_dwordx4 v[80:83], v[4:5], off offset:256
	global_load_dwordx4 v[84:87], v[4:5], off offset:320
	global_load_dwordx4 v[88:91], v[4:5], off offset:384
	global_load_dwordx4 v[92:95], v[4:5], off offset:448
	s_waitcnt vmcnt(0)
	s_waitcnt lgkmcnt(0)
	s_barrier
	v_add_u32_e32 v188, v150, v151
	v_add_u32_e32 v187, v150, v152
	v_add_u32_e32 v186, v150, v153
	v_add_u32_e32 v137, v150, v154
	v_add_u32_e32 v135, v150, v151
	v_add_u32_e32 v135, 0x10000, v135
	v_add_u32_e32 v159, v150, v152
	v_add_u32_e32 v159, 0x10000, v159
	v_add_u32_e32 v176, v150, v153
	v_add_u32_e32 v176, 0x10000, v176
	v_add_u32_e32 v177, v150, v154
	v_add_u32_e32 v177, 0x10000, v177
	ds_read_b128 v[100:103], v188
	ds_read_b128 v[160:163], v187
	ds_read_b128 v[164:167], v186
	ds_read_b128 v[168:171], v137
	ds_read_b128 v[172:175], v188 offset:256
	ds_read_b128 v[204:207], v187 offset:256
	ds_read_b128 v[208:211], v186 offset:256
	ds_read_b128 v[212:215], v137 offset:256
	s_mov_b32 s11, s10
	s_mov_b32 m0, s29
	s_add_i32 s20, s20, s38
	s_ashr_i32 s0, s20, 31
	s_lshr_b32 s0, s0, 25
	s_add_i32 s0, s20, s0
	s_ashr_i32 s1, s0, 7
	s_and_b32 s0, s0, 0xff80
	s_sub_i32 s0, s20, s0
	s_cmp_eq_u32 s100, 1
	s_cbranch_scc0 .Lqo_p4b3
	s_mov_b32 s1, s99
	s_lshr_b32 s0, s20, 8
	s_add_i32 s0, s0, s98
	s_add_i32 s0, s0, s98

.LBB0_1171:
	s_cmp_eq_u32 s100, 1
	s_cbranch_scc1 .Lqs8
	s_cmp_gt_i32 s91, 9
	s_cselect_b64 s[2:3], -1, 0
	s_and_b64 s[0:1], s[4:5], s[2:3]
	s_andn2_b64 vcc, exec, s[0:1]
	s_cbranch_vccnz .LBB0_1227
	s_cmp_gt_u32 s80, 63
	s_waitcnt lgkmcnt(0)
	s_mov_b64 s[8:9], 0
	s_cbranch_scc1 .LBB0_1174
	v_mbcnt_hi_u32_b32 v0, -1, v217
	v_cmp_eq_u32_e32 vcc, 0, v0
	s_and_b64 s[8:9], vcc, exec

.LBB0_1227:
	s_cmp_eq_u32 s100, 1
	s_cbranch_scc0 .Lqo_p6
	s_lshl_b32 s6, s98, 2
	s_add_i32 s6, s6, s99

.Lqs7:
	s_waitcnt vmcnt(0) lgkmcnt(0)
	s_barrier
	s_cmp_gt_u32 s80, 63
	s_cbranch_scc1 .Lqs7_wait
	s_add_u32 s8, s18, 0xc0000
	s_addc_u32 s9, s19, 0
	s_mov_b64 s[10:11], exec
	s_mov_b64 exec, 1
	s_lshl_b32 s0, s98, 8
	s_add_i32 s0, s0, 96
	v_mov_b32_e32 v0, s0
	v_mov_b32_e32 v1, 1
	global_atomic_add v0, v1, s[8:9]
	buffer_inv sc1
	s_mov_b32 s1, 0

.Lqs5:
	s_waitcnt vmcnt(0) lgkmcnt(0)
	s_barrier
	s_cmp_gt_u32 s80, 63
	s_cbranch_scc1 .Lqs5_wait
	s_add_u32 s8, s18, 0xc0000
	s_addc_u32 s9, s19, 0
	s_mov_b64 s[10:11], exec
	s_mov_b64 exec, 1
	s_lshl_b32 s0, s98, 8
	s_add_i32 s0, s0, 32
	v_mov_b32_e32 v0, s0
	v_mov_b32_e32 v1, 1
	global_atomic_add v0, v1, s[8:9]
	buffer_inv sc1
	s_mov_b32 s1, 0

.Lqs8:
	s_waitcnt vmcnt(0) lgkmcnt(0)
	s_barrier
	s_cmp_gt_u32 s80, 63
	s_cbranch_scc1 .Lqs8_wait
	s_add_u32 s8, s18, 0xc0000
	s_addc_u32 s9, s19, 0
	s_mov_b64 s[10:11], exec
	s_mov_b64 exec, 1
	s_lshl_b32 s0, s98, 8
	s_add_i32 s0, s0, 128
	v_mov_b32_e32 v0, s0
	v_mov_b32_e32 v1, 1
	global_atomic_add v0, v1, s[8:9]
	buffer_inv sc1
	s_mov_b32 s1, 0

.Lqs4:
	s_and_b32 s0, s79, 31
	s_lshl_b32 s0, s0, 3
	s_lshr_b32 s1, s79, 5
	s_add_i32 s6, s0, s1
	s_lshl_b32 s0, s79, 3
	s_add_i32 s36, s0, s88
	s_waitcnt vmcnt(0) lgkmcnt(0)
	s_barrier
	s_cmp_gt_u32 s80, 63
	s_cbranch_scc1 .Lqs4_wait
	s_add_u32 s8, s18, 0xc0000
	s_addc_u32 s9, s19, 0
	s_mov_b64 s[10:11], exec
	s_mov_b64 exec, 1
	s_lshl_b32 s0, s98, 8
	s_add_i32 s0, s0, 0
	v_mov_b32_e32 v0, s0
	v_mov_b32_e32 v1, 1
	global_atomic_add v0, v1, s[8:9]
	buffer_inv sc1
	s_mov_b32 s1, 0
